# v73 with the 15 hot loop heads (11 GEMM K-loops, 4 attention loops) aligned to 64 bytes
# baseline (speedup 1.0000x reference)
; #define PG8_BAR __builtin_amdgcn_s_barrier()
; template <class Epi, class Sched, bool PERM, bool FP8 = false, bool GATHER = false>
; DI void gemm_phase(LAS unsigned char* lds, const unsigned char* wsb, const unsigned lda, const unsigned ldb, const int nt, const Sched& S, const Epi& E) {
;     ...
; #pragma unroll
;         for (int a = 0; a < 2; ++a)
; #pragma unroll
;             for (int b = 0; b < 2; ++b)
; #pragma unroll
;                 for (int m = 0; m < 4; ++m)
; #pragma unroll
;                     for (int n = 0; n < 2; ++n) acc[a][b][m][n] = (f32x4){0.f, 0.f, 0.f, 0.f};
;         cur = nxt; cA = nA; cB = nB; ++ui;
;         if (wr == 1) PG8_BAR;
.LBB0_404:
	v_mov_b32_e32 v2, 0
	s_add_i32 s4, s40, 0x100
	s_add_i32 s5, s7, 0x20080
	s_mov_b32 s7, -2
	v_mov_b32_e32 v3, v2
	v_mov_b32_e32 v4, v2
	v_mov_b32_e32 v5, v2
	v_mov_b32_e32 v6, v2
	v_mov_b32_e32 v7, v2
	v_mov_b32_e32 v8, v2
	v_mov_b32_e32 v9, v2
	v_mov_b32_e32 v18, v2
	v_mov_b32_e32 v19, v2
	v_mov_b32_e32 v20, v2
	v_mov_b32_e32 v21, v2
	v_mov_b32_e32 v22, v2
	v_mov_b32_e32 v23, v2
	v_mov_b32_e32 v24, v2
	v_mov_b32_e32 v25, v2
	v_mov_b32_e32 v34, v2
	v_mov_b32_e32 v35, v2
	v_mov_b32_e32 v36, v2
	v_mov_b32_e32 v37, v2
	v_mov_b32_e32 v38, v2
	v_mov_b32_e32 v39, v2
	v_mov_b32_e32 v40, v2
	v_mov_b32_e32 v41, v2
	v_mov_b32_e32 v50, v2
	v_mov_b32_e32 v51, v2
	v_mov_b32_e32 v52, v2
	v_mov_b32_e32 v53, v2
	v_mov_b32_e32 v54, v2
	v_mov_b32_e32 v55, v2
	v_mov_b32_e32 v56, v2
	v_mov_b32_e32 v57, v2
	s_waitcnt vmcnt(0)
	v_mov_b32_e32 v10, v2
	v_mov_b32_e32 v11, v2
	v_mov_b32_e32 v12, v2
	v_mov_b32_e32 v13, v2
	v_mov_b32_e32 v14, v2
	v_mov_b32_e32 v15, v2
	v_mov_b32_e32 v16, v2
	v_mov_b32_e32 v17, v2
	v_mov_b32_e32 v26, v2
	v_mov_b32_e32 v27, v2
	v_mov_b32_e32 v28, v2
	v_mov_b32_e32 v29, v2
	v_mov_b32_e32 v30, v2
	v_mov_b32_e32 v31, v2
	v_mov_b32_e32 v32, v2
	v_mov_b32_e32 v33, v2
	v_mov_b32_e32 v42, v2
	v_mov_b32_e32 v43, v2
	v_mov_b32_e32 v44, v2
	v_mov_b32_e32 v45, v2
	v_mov_b32_e32 v46, v2
	v_mov_b32_e32 v47, v2
	v_mov_b32_e32 v48, v2
	v_mov_b32_e32 v49, v2
	v_mov_b32_e32 v58, v2
	v_mov_b32_e32 v59, v2
	v_mov_b32_e32 v60, v2
	v_mov_b32_e32 v61, v2
	v_mov_b32_e32 v62, v2
	v_mov_b32_e32 v63, v2
	v_mov_b32_e32 v64, v2
	v_mov_b32_e32 v65, v2
	v_mov_b32_e32 v66, v2
	v_mov_b32_e32 v67, v2
	v_mov_b32_e32 v68, v2
	v_mov_b32_e32 v69, v2
	v_mov_b32_e32 v70, v2
	v_mov_b32_e32 v71, v2
	v_mov_b32_e32 v72, v2
	v_mov_b32_e32 v73, v2
	v_mov_b32_e32 v82, v2
	v_mov_b32_e32 v83, v2
	v_mov_b32_e32 v84, v2
	v_mov_b32_e32 v85, v2
	v_mov_b32_e32 v86, v2
	v_mov_b32_e32 v87, v2
	v_mov_b32_e32 v88, v2
	v_mov_b32_e32 v89, v2
	v_mov_b32_e32 v98, v2
	v_mov_b32_e32 v99, v2
	v_mov_b32_e32 v100, v2
	v_mov_b32_e32 v101, v2
	v_mov_b32_e32 v102, v2
	v_mov_b32_e32 v103, v2
	v_mov_b32_e32 v104, v2
	v_mov_b32_e32 v105, v2
	v_mov_b32_e32 v114, v2
	v_mov_b32_e32 v115, v2
	v_mov_b32_e32 v116, v2
	v_mov_b32_e32 v117, v2
	v_mov_b32_e32 v118, v2
	v_mov_b32_e32 v119, v2
	v_mov_b32_e32 v120, v2
	v_mov_b32_e32 v121, v2
	v_mov_b32_e32 v74, v2
	v_mov_b32_e32 v75, v2
	v_mov_b32_e32 v76, v2
	v_mov_b32_e32 v77, v2
	v_mov_b32_e32 v78, v2
	v_mov_b32_e32 v79, v2
	v_mov_b32_e32 v80, v2
	v_mov_b32_e32 v81, v2
	v_mov_b32_e32 v90, v2
	v_mov_b32_e32 v91, v2
	v_mov_b32_e32 v92, v2
	v_mov_b32_e32 v93, v2
	v_mov_b32_e32 v94, v2
	v_mov_b32_e32 v95, v2
	v_mov_b32_e32 v96, v2
	v_mov_b32_e32 v97, v2
	v_mov_b32_e32 v106, v2
	v_mov_b32_e32 v107, v2
	v_mov_b32_e32 v108, v2
	v_mov_b32_e32 v109, v2
	v_mov_b32_e32 v110, v2
	v_mov_b32_e32 v111, v2
	v_mov_b32_e32 v112, v2
	v_mov_b32_e32 v113, v2
	v_mov_b32_e32 v122, v2
	v_mov_b32_e32 v123, v2
	v_mov_b32_e32 v124, v2
	v_mov_b32_e32 v125, v2
	v_mov_b32_e32 v126, v2
	v_mov_b32_e32 v127, v2
	v_mov_b32_e32 v128, v2
	v_mov_b32_e32 v129, v2
	.p2align	6

; #define PG8_BAR __builtin_amdgcn_s_barrier()
; template <class Epi, class Sched, bool PERM, bool FP8 = false, bool GATHER = false>
; DI void gemm_phase(LAS unsigned char* lds, const unsigned char* wsb, const unsigned lda, const unsigned ldb, const int nt, const Sched& S, const Epi& E) {
;     ...
; #pragma unroll
;         for (int a = 0; a < 2; ++a)
; #pragma unroll
;             for (int b = 0; b < 2; ++b)
; #pragma unroll
;                 for (int m = 0; m < 4; ++m)
; #pragma unroll
;                     for (int n = 0; n < 2; ++n) acc[a][b][m][n] = (f32x4){0.f, 0.f, 0.f, 0.f};
;         cur = nxt; cA = nA; cB = nB; ++ui;
;         if (wr == 1) PG8_BAR;
.LBB0_572:
	v_mov_b32_e32 v2, 0
	s_addk_i32 s18, 0x100
	s_add_i32 s19, s19, 0x20080
	s_mov_b32 s20, -2
	v_mov_b32_e32 v3, v2
	v_mov_b32_e32 v4, v2
	v_mov_b32_e32 v5, v2
	v_mov_b32_e32 v6, v2
	v_mov_b32_e32 v7, v2
	v_mov_b32_e32 v8, v2
	v_mov_b32_e32 v9, v2
	v_mov_b32_e32 v14, v2
	v_mov_b32_e32 v15, v2
	v_mov_b32_e32 v16, v2
	v_mov_b32_e32 v17, v2
	v_mov_b32_e32 v22, v2
	v_mov_b32_e32 v23, v2
	v_mov_b32_e32 v24, v2
	v_mov_b32_e32 v25, v2
	v_mov_b32_e32 v30, v2
	v_mov_b32_e32 v31, v2
	v_mov_b32_e32 v32, v2
	v_mov_b32_e32 v33, v2
	v_mov_b32_e32 v38, v2
	v_mov_b32_e32 v39, v2
	v_mov_b32_e32 v40, v2
	v_mov_b32_e32 v41, v2
	v_mov_b32_e32 v46, v2
	v_mov_b32_e32 v47, v2
	v_mov_b32_e32 v48, v2
	v_mov_b32_e32 v49, v2
	v_mov_b32_e32 v54, v2
	v_mov_b32_e32 v55, v2
	v_mov_b32_e32 v56, v2
	v_mov_b32_e32 v57, v2
	v_mov_b32_e32 v10, v2
	v_mov_b32_e32 v11, v2
	v_mov_b32_e32 v12, v2
	v_mov_b32_e32 v13, v2
	v_mov_b32_e32 v18, v2
	v_mov_b32_e32 v19, v2
	v_mov_b32_e32 v20, v2
	v_mov_b32_e32 v21, v2
	v_mov_b32_e32 v26, v2
	v_mov_b32_e32 v27, v2
	v_mov_b32_e32 v28, v2
	v_mov_b32_e32 v29, v2
	v_mov_b32_e32 v34, v2
	v_mov_b32_e32 v35, v2
	v_mov_b32_e32 v36, v2
	v_mov_b32_e32 v37, v2
	v_mov_b32_e32 v42, v2
	v_mov_b32_e32 v43, v2
	v_mov_b32_e32 v44, v2
	v_mov_b32_e32 v45, v2
	v_mov_b32_e32 v50, v2
	v_mov_b32_e32 v51, v2
	v_mov_b32_e32 v52, v2
	v_mov_b32_e32 v53, v2
	v_mov_b32_e32 v58, v2
	v_mov_b32_e32 v59, v2
	v_mov_b32_e32 v60, v2
	v_mov_b32_e32 v61, v2
	v_mov_b32_e32 v62, v2
	v_mov_b32_e32 v63, v2
	v_mov_b32_e32 v64, v2
	v_mov_b32_e32 v65, v2
	v_mov_b32_e32 v66, v2
	v_mov_b32_e32 v67, v2
	v_mov_b32_e32 v68, v2
	v_mov_b32_e32 v69, v2
	v_mov_b32_e32 v70, v2
	v_mov_b32_e32 v71, v2
	v_mov_b32_e32 v72, v2
	v_mov_b32_e32 v73, v2
	v_mov_b32_e32 v78, v2
	v_mov_b32_e32 v79, v2
	v_mov_b32_e32 v80, v2
	v_mov_b32_e32 v81, v2
	v_mov_b32_e32 v86, v2
	v_mov_b32_e32 v87, v2
	v_mov_b32_e32 v88, v2
	v_mov_b32_e32 v89, v2
	v_mov_b32_e32 v94, v2
	v_mov_b32_e32 v95, v2
	v_mov_b32_e32 v96, v2
	v_mov_b32_e32 v97, v2
	v_mov_b32_e32 v102, v2
	v_mov_b32_e32 v103, v2
	v_mov_b32_e32 v104, v2
	v_mov_b32_e32 v105, v2
	v_mov_b32_e32 v110, v2
	v_mov_b32_e32 v111, v2
	v_mov_b32_e32 v112, v2
	v_mov_b32_e32 v113, v2
	v_mov_b32_e32 v118, v2
	v_mov_b32_e32 v119, v2
	v_mov_b32_e32 v120, v2
	v_mov_b32_e32 v121, v2
	v_mov_b32_e32 v74, v2
	v_mov_b32_e32 v75, v2
	v_mov_b32_e32 v76, v2
	v_mov_b32_e32 v77, v2
	v_mov_b32_e32 v82, v2
	v_mov_b32_e32 v83, v2
	v_mov_b32_e32 v84, v2
	v_mov_b32_e32 v85, v2
	v_mov_b32_e32 v90, v2
	v_mov_b32_e32 v91, v2
	v_mov_b32_e32 v92, v2
	v_mov_b32_e32 v93, v2
	v_mov_b32_e32 v98, v2
	v_mov_b32_e32 v99, v2
	v_mov_b32_e32 v100, v2
	v_mov_b32_e32 v101, v2
	v_mov_b32_e32 v106, v2
	v_mov_b32_e32 v107, v2
	v_mov_b32_e32 v108, v2
	v_mov_b32_e32 v109, v2
	v_mov_b32_e32 v114, v2
	v_mov_b32_e32 v115, v2
	v_mov_b32_e32 v116, v2
	v_mov_b32_e32 v117, v2
	v_mov_b32_e32 v122, v2
	v_mov_b32_e32 v123, v2
	v_mov_b32_e32 v124, v2
	v_mov_b32_e32 v125, v2
	v_mov_b32_e32 v126, v2
	v_mov_b32_e32 v127, v2
	v_mov_b32_e32 v128, v2
	v_mov_b32_e32 v129, v2
	.p2align	6

; DI void attn_unit_d8(unsigned char* lds, const AttnArgs& a) {
;     ...
;     f32x16 o0[2], o1[2];
; #pragma unroll
;     for (int d = 0; d < 2; ++d) { o0[d] = (f32x16){}; o1[d] = (f32x16){}; }
;     f32x4 l0 = {0.f, 0.f, 0.f, 0.f}, l1 = {0.f, 0.f, 0.f, 0.f};
;     constexpr int D8_SLOT = 2 * 64 * A8_PITCH;
;     u32x2 kreg0, vreg0, kreg1, vreg1;
;     auto gload = [&](int t, u32x2& kreg, u32x2& vreg) __attribute__((always_inline)) {
;         const unsigned char* kp = (t < 64) ? a.klat8 + (size_t)(t * 64 + lrow) * 256 : a.kctx8 + (size_t)((t - 64) * 64 + lrow) * 256;
;         kreg = *(const u32x2*)(kp + 8 * lch);
;         vreg = *(const u32x2*)(vsrc + (size_t)t * 64);
;     };
;     auto lstore = [&](int slot, const u32x2& kreg, const u32x2& vreg) __attribute__((always_inline)) { unsigned char* b = lds + slot * D8_SLOT;
;         *(u32x2*)(b + ldst) = kreg; *(unsigned*)(b + ldv) = vreg.x; *(unsigned*)(b + ldv + 32) = vreg.y; };
;     auto rd32 = [&](const unsigned char* p) __attribute__((always_inline)) -> v8i { const u32x4 lo = *(const u32x4*)p, hi = *(const u32x4*)(p + 16);
;         return (v8i){(int)lo.x, (int)lo.y, (int)lo.z, (int)lo.w, (int)hi.x, (int)hi.y, (int)hi.z, (int)hi.w}; };
;     auto expsum = [&](f32x16& sc, f32x4& l) __attribute__((always_inline)) {
; #pragma unroll
;         for (int i = 0; i < 16; ++i) sc[i] = __builtin_amdgcn_exp2f(sc[i]);
; #pragma unroll
;         for (int i = 0; i < 4; ++i) l += (f32x4){sc[4 * i], sc[4 * i + 1], sc[4 * i + 2], sc[4 * i + 3]};
;     };
;     auto pack8 = [&](const f32x16& s0, const f32x16& s1) __attribute__((always_inline)) -> v8i { v8i p;
; #pragma unroll
;         for (int g = 0; g < 4; ++g) { p[g] = (int)pk4_fp8_div16(s0[4 * g], s0[4 * g + 1], s0[4 * g + 2], s0[4 * g + 3]); p[4 + g] = (int)pk4_fp8_div16(s1[4 * g], s1[4 * g + 1], s1[4 * g + 2], s1[4 * g + 3]); }
;         return p; };
;     auto pack4 = [&](const f32x16& sc, v8i& p, const int o) __attribute__((always_inline)) {
; #pragma unroll
;         for (int g = 0; g < 4; ++g) p[o + g] = (int)pk4_fp8_div16(sc[4 * g], sc[4 * g + 1], sc[4 * g + 2], sc[4 * g + 3]); };
;     auto qk = [&](const unsigned char* Kb, int hh, f32x16& sa, f32x16& sb) __attribute__((always_inline)) { const v8i kf = rd32(Kb + koff + hh * 32 * A8_PITCH);
;         sa = mfma8(kf, qfa, (f32x16){}); sb = mfma8(kf, qfb, (f32x16){}); };
.LBB0_662:
	s_and_b32 s61, s42, 1
	s_lshl_b32 s61, s61, 3
	s_sub_i32 s61, 0, s61
	v_mov_b32_e32 v2, 0
	s_mov_b32 s16, 0
	v_mov_b32_e32 v138, 0
	v_mov_b32_e32 v139, 0
	v_mov_b32_e32 v140, 0
	v_mov_b32_e32 v141, 0
	v_mov_b32_e32 v142, 0
	v_mov_b32_e32 v143, 0
	v_mov_b32_e32 v144, 0
	v_mov_b32_e32 v145, 0
	v_mov_b32_e32 v130, 0
	v_mov_b32_e32 v131, 0
	v_mov_b32_e32 v132, 0
	v_mov_b32_e32 v133, 0
	v_mov_b32_e32 v134, 0
	v_mov_b32_e32 v135, 0
	v_mov_b32_e32 v136, 0
	v_mov_b32_e32 v137, 0
	v_mov_b32_e32 v154, 0
	v_mov_b32_e32 v155, 0
	v_mov_b32_e32 v156, 0
	v_mov_b32_e32 v157, 0
	v_mov_b32_e32 v158, 0
	v_mov_b32_e32 v159, 0
	v_mov_b32_e32 v160, 0
	v_mov_b32_e32 v161, 0
	v_mov_b32_e32 v146, 0
	v_mov_b32_e32 v147, 0
	v_mov_b32_e32 v148, 0
	v_mov_b32_e32 v149, 0
	v_mov_b32_e32 v150, 0
	v_mov_b32_e32 v151, 0
	v_mov_b32_e32 v152, 0
	v_mov_b32_e32 v153, 0
	v_mov_b32_e32 v3, v2
	v_mov_b32_e32 v4, v2
	v_mov_b32_e32 v5, v2
	v_mov_b32_e32 v6, v2
	v_mov_b32_e32 v7, v2
	v_mov_b32_e32 v8, v2
	v_mov_b32_e32 v9, v2
	v_mov_b32_e32 v10, v2
	v_mov_b32_e32 v11, v2
	v_mov_b32_e32 v12, v2
	v_mov_b32_e32 v13, v2
	v_mov_b32_e32 v14, v2
	v_mov_b32_e32 v15, v2
	v_mov_b32_e32 v16, v2
	v_mov_b32_e32 v17, v2
	v_mov_b32_e32 v18, v2
	v_mov_b32_e32 v19, v2
	v_mov_b32_e32 v20, v2
	v_mov_b32_e32 v21, v2
	v_mov_b32_e32 v22, v2
	v_mov_b32_e32 v23, v2
	v_mov_b32_e32 v24, v2
	v_mov_b32_e32 v25, v2
	v_mov_b32_e32 v26, v2
	v_mov_b32_e32 v27, v2
	v_mov_b32_e32 v28, v2
	v_mov_b32_e32 v29, v2
	v_mov_b32_e32 v30, v2
	v_mov_b32_e32 v31, v2
	v_mov_b32_e32 v32, v2
	v_mov_b32_e32 v33, v2
	v_mov_b32_e32 v50, v2
	v_mov_b32_e32 v51, v2
	v_mov_b32_e32 v52, v2
	v_mov_b32_e32 v53, v2
	v_mov_b32_e32 v54, v2
	v_mov_b32_e32 v55, v2
	v_mov_b32_e32 v56, v2
	v_mov_b32_e32 v57, v2
	v_mov_b32_e32 v58, v2
	v_mov_b32_e32 v59, v2
	v_mov_b32_e32 v60, v2
	v_mov_b32_e32 v61, v2
	v_mov_b32_e32 v62, v2
	v_mov_b32_e32 v63, v2
	v_mov_b32_e32 v64, v2
	v_mov_b32_e32 v65, v2
	v_mov_b32_e32 v34, v2
	v_mov_b32_e32 v35, v2
	v_mov_b32_e32 v36, v2
	v_mov_b32_e32 v37, v2
	v_mov_b32_e32 v38, v2
	v_mov_b32_e32 v39, v2
	v_mov_b32_e32 v40, v2
	v_mov_b32_e32 v41, v2
	v_mov_b32_e32 v42, v2
	v_mov_b32_e32 v43, v2
	v_mov_b32_e32 v44, v2
	v_mov_b32_e32 v45, v2
	v_mov_b32_e32 v46, v2
	v_mov_b32_e32 v47, v2
	v_mov_b32_e32 v48, v2
	v_mov_b32_e32 v49, v2
	v_mov_b32_e32 v186, v2
	v_mov_b32_e32 v187, v2
	v_mov_b32_e32 v184, v2
	v_mov_b32_e32 v185, v2
	v_mov_b32_e32 v190, v2
	v_mov_b32_e32 v191, v2
	v_mov_b32_e32 v188, v2
	v_mov_b32_e32 v189, v2
	.p2align	6

; DI void attn_unit_a8(unsigned char* lds, const AttnArgs& a) {
;     ...
;     {
;         int t = a.t0;
;         if (wrider)
;             for (int j = 0; j < AT_NWT; ++j, t += 2) { step(t, kregB, vregB, kregA, vregA, sx0, sx1, sy0, sy1, 1, j); step(t + 1, kregA, vregA, kregB, vregB, sy0, sy1, sx0, sx1, 2, j); }
;         for (; t < a.t1; t += 2) {
;             step(t, kregB, vregB, kregA, vregA, sx0, sx1, sy0, sy1, 0, 0);
;             if (t + 1 < a.t1) step(t + 1, kregA, vregA, kregB, vregB, sy0, sy1, sx0, sx1, 0, 0);
;             else { sx0 = sy0; sx1 = sy1; }
;         }
.LBB0_712:
	s_cmpk_gt_i32 s56, 0x43
	s_cbranch_scc1 .LBB0_688
	s_mov_b32 s8, 0
	v_mov_b64_e32 v[80:81], v[48:49]
	v_mov_b64_e32 v[78:79], v[46:47]
	v_mov_b64_e32 v[76:77], v[44:45]
	v_mov_b64_e32 v[74:75], v[42:43]
	v_mov_b64_e32 v[72:73], v[40:41]
	v_mov_b64_e32 v[70:71], v[38:39]
	v_mov_b64_e32 v[68:69], v[36:37]
	v_mov_b64_e32 v[66:67], v[34:35]
	v_mov_b64_e32 v[96:97], v[64:65]
	v_mov_b64_e32 v[94:95], v[62:63]
	v_mov_b64_e32 v[92:93], v[60:61]
	v_mov_b64_e32 v[90:91], v[58:59]
	v_mov_b64_e32 v[88:89], v[56:57]
	v_mov_b64_e32 v[86:87], v[54:55]
	v_mov_b64_e32 v[84:85], v[52:53]
	v_mov_b64_e32 v[82:83], v[50:51]
	v_mov_b32_e32 v236, v154
	v_ashrrev_i32_e32 v237, 31, v154
	v_lshlrev_b64 v[236:237], 7, v[236:237]
	v_lshl_add_u64 v[236:237], v[236:237], 0, v[130:131]
	.p2align	6

; #define PG8_BAR __builtin_amdgcn_s_barrier()
; template <class Epi, class Sched, bool PERM, bool FP8 = false, bool GATHER = false>
; DI void gemm_phase(LAS unsigned char* lds, const unsigned char* wsb, const unsigned lda, const unsigned ldb, const int nt, const Sched& S, const Epi& E) {
;     ...
; #pragma unroll
;         for (int a = 0; a < 2; ++a)
; #pragma unroll
;             for (int b = 0; b < 2; ++b)
; #pragma unroll
;                 for (int m = 0; m < 4; ++m)
; #pragma unroll
;                     for (int n = 0; n < 2; ++n) acc[a][b][m][n] = (f32x4){0.f, 0.f, 0.f, 0.f};
;         cur = nxt; cA = nA; cB = nB; ++ui;
;         if (wr == 1) PG8_BAR;
;         u.pm = 0; u.pn = 0; u.e = NLAT + L * CTX; u.A = (unsigned)WS_TC; u.B = (unsigned)WS_FTC + (unsigned)L * (256u * 1024u); return true; }
.LBB0_724:
	s_add_i32 s79, s79, 1
	s_mov_b32 s54, s29
	s_mul_i32 s29, s79, s64
	s_mov_b32 s81, s80
	s_add_i32 s80, s29, s28
	s_lshl_b32 s29, s80, 18
	s_add_i32 s29, s29, 0x2abd4000
	s_cmp_lt_i32 s80, 8
	s_cselect_b64 s[40:41], -1, 0
	s_and_b64 s[42:43], s[40:41], exec
	v_mov_b32_e32 v2, 0
	s_cselect_b32 s82, s29, s54
	s_add_u32 s83, s54, 0x100
	s_mov_b32 s84, -2
	s_mov_b64 s[42:43], 0
	v_mov_b32_e32 v3, v2
	v_mov_b32_e32 v4, v2
	v_mov_b32_e32 v5, v2
	v_mov_b32_e32 v6, v2
	v_mov_b32_e32 v7, v2
	v_mov_b32_e32 v8, v2
	v_mov_b32_e32 v9, v2
	v_mov_b32_e32 v18, v2
	v_mov_b32_e32 v19, v2
	v_mov_b32_e32 v20, v2
	v_mov_b32_e32 v21, v2
	v_mov_b32_e32 v22, v2
	v_mov_b32_e32 v23, v2
	v_mov_b32_e32 v24, v2
	v_mov_b32_e32 v25, v2
	v_mov_b32_e32 v34, v2
	v_mov_b32_e32 v35, v2
	v_mov_b32_e32 v36, v2
	v_mov_b32_e32 v37, v2
	v_mov_b32_e32 v38, v2
	v_mov_b32_e32 v39, v2
	v_mov_b32_e32 v40, v2
	v_mov_b32_e32 v41, v2
	v_mov_b32_e32 v50, v2
	v_mov_b32_e32 v51, v2
	v_mov_b32_e32 v52, v2
	v_mov_b32_e32 v53, v2
	v_mov_b32_e32 v54, v2
	v_mov_b32_e32 v55, v2
	v_mov_b32_e32 v56, v2
	v_mov_b32_e32 v57, v2
	v_mov_b32_e32 v10, v2
	v_mov_b32_e32 v11, v2
	v_mov_b32_e32 v12, v2
	v_mov_b32_e32 v13, v2
	v_mov_b32_e32 v14, v2
	v_mov_b32_e32 v15, v2
	v_mov_b32_e32 v16, v2
	v_mov_b32_e32 v17, v2
	v_mov_b32_e32 v26, v2
	v_mov_b32_e32 v27, v2
	v_mov_b32_e32 v28, v2
	v_mov_b32_e32 v29, v2
	v_mov_b32_e32 v30, v2
	v_mov_b32_e32 v31, v2
	v_mov_b32_e32 v32, v2
	v_mov_b32_e32 v33, v2
	v_mov_b32_e32 v42, v2
	v_mov_b32_e32 v43, v2
	v_mov_b32_e32 v44, v2
	v_mov_b32_e32 v45, v2
	v_mov_b32_e32 v46, v2
	v_mov_b32_e32 v47, v2
	v_mov_b32_e32 v48, v2
	v_mov_b32_e32 v49, v2
	v_mov_b32_e32 v58, v2
	v_mov_b32_e32 v59, v2
	v_mov_b32_e32 v60, v2
	v_mov_b32_e32 v61, v2
	v_mov_b32_e32 v62, v2
	v_mov_b32_e32 v63, v2
	v_mov_b32_e32 v64, v2
	v_mov_b32_e32 v65, v2
	v_mov_b32_e32 v66, v2
	v_mov_b32_e32 v67, v2
	v_mov_b32_e32 v68, v2
	v_mov_b32_e32 v69, v2
	v_mov_b32_e32 v70, v2
	v_mov_b32_e32 v71, v2
	v_mov_b32_e32 v72, v2
	v_mov_b32_e32 v73, v2
	v_mov_b32_e32 v82, v2
	v_mov_b32_e32 v83, v2
	v_mov_b32_e32 v84, v2
	v_mov_b32_e32 v85, v2
	v_mov_b32_e32 v86, v2
	v_mov_b32_e32 v87, v2
	v_mov_b32_e32 v88, v2
	v_mov_b32_e32 v89, v2
	v_mov_b32_e32 v98, v2
	v_mov_b32_e32 v99, v2
	v_mov_b32_e32 v100, v2
	v_mov_b32_e32 v101, v2
	v_mov_b32_e32 v102, v2
	v_mov_b32_e32 v103, v2
	v_mov_b32_e32 v104, v2
	v_mov_b32_e32 v105, v2
	v_mov_b32_e32 v114, v2
	v_mov_b32_e32 v115, v2
	v_mov_b32_e32 v116, v2
	v_mov_b32_e32 v117, v2
	v_mov_b32_e32 v118, v2
	v_mov_b32_e32 v119, v2
	v_mov_b32_e32 v120, v2
	v_mov_b32_e32 v121, v2
	v_mov_b32_e32 v74, v2
	v_mov_b32_e32 v75, v2
	v_mov_b32_e32 v76, v2
	v_mov_b32_e32 v77, v2
	v_mov_b32_e32 v78, v2
	v_mov_b32_e32 v79, v2
	v_mov_b32_e32 v80, v2
	v_mov_b32_e32 v81, v2
	v_mov_b32_e32 v90, v2
	v_mov_b32_e32 v91, v2
	v_mov_b32_e32 v92, v2
	v_mov_b32_e32 v93, v2
	v_mov_b32_e32 v94, v2
	v_mov_b32_e32 v95, v2
	v_mov_b32_e32 v96, v2
	v_mov_b32_e32 v97, v2
	v_mov_b32_e32 v106, v2
	v_mov_b32_e32 v107, v2
	v_mov_b32_e32 v108, v2
	v_mov_b32_e32 v109, v2
	v_mov_b32_e32 v110, v2
	v_mov_b32_e32 v111, v2
	v_mov_b32_e32 v112, v2
	v_mov_b32_e32 v113, v2
	v_mov_b32_e32 v122, v2
	v_mov_b32_e32 v123, v2
	v_mov_b32_e32 v124, v2
	v_mov_b32_e32 v125, v2
	v_mov_b32_e32 v126, v2
	v_mov_b32_e32 v127, v2
	v_mov_b32_e32 v128, v2
	v_mov_b32_e32 v129, v2
	.p2align	6

; #define PG8_BAR __builtin_amdgcn_s_barrier()
; template <class Epi, class Sched, bool PERM, bool FP8 = false, bool GATHER = false>
; DI void gemm_phase(LAS unsigned char* lds, const unsigned char* wsb, const unsigned lda, const unsigned ldb, const int nt, const Sched& S, const Epi& E) {
;     ...
; #pragma unroll
;         for (int a = 0; a < 2; ++a)
; #pragma unroll
;             for (int b = 0; b < 2; ++b)
; #pragma unroll
;                 for (int m = 0; m < 4; ++m)
; #pragma unroll
;                     for (int n = 0; n < 2; ++n) acc[a][b][m][n] = (f32x4){0.f, 0.f, 0.f, 0.f};
;         cur = nxt; cA = nA; cB = nB; ++ui;
;         if (wr == 1) PG8_BAR;
.LBB0_909:
	v_mov_b32_e32 v2, 0
	s_add_i32 s21, s21, 0x20080
	s_addk_i32 s22, 0x100
	s_mov_b32 s23, -2
	v_mov_b32_e32 v3, v2
	v_mov_b32_e32 v4, v2
	v_mov_b32_e32 v5, v2
	v_mov_b32_e32 v6, v2
	v_mov_b32_e32 v7, v2
	v_mov_b32_e32 v8, v2
	v_mov_b32_e32 v9, v2
	v_mov_b32_e32 v10, v2
	v_mov_b32_e32 v11, v2
	v_mov_b32_e32 v12, v2
	v_mov_b32_e32 v13, v2
	v_mov_b32_e32 v18, v2
	v_mov_b32_e32 v19, v2
	v_mov_b32_e32 v20, v2
	v_mov_b32_e32 v21, v2
	v_mov_b32_e32 v26, v2
	v_mov_b32_e32 v27, v2
	v_mov_b32_e32 v28, v2
	v_mov_b32_e32 v29, v2
	v_mov_b32_e32 v34, v2
	v_mov_b32_e32 v35, v2
	v_mov_b32_e32 v36, v2
	v_mov_b32_e32 v37, v2
	v_mov_b32_e32 v46, v2
	v_mov_b32_e32 v47, v2
	v_mov_b32_e32 v48, v2
	v_mov_b32_e32 v49, v2
	v_mov_b32_e32 v54, v2
	v_mov_b32_e32 v55, v2
	v_mov_b32_e32 v56, v2
	v_mov_b32_e32 v57, v2
	v_mov_b32_e32 v14, v2
	v_mov_b32_e32 v15, v2
	v_mov_b32_e32 v16, v2
	v_mov_b32_e32 v17, v2
	v_mov_b32_e32 v22, v2
	v_mov_b32_e32 v23, v2
	v_mov_b32_e32 v24, v2
	v_mov_b32_e32 v25, v2
	v_mov_b32_e32 v30, v2
	v_mov_b32_e32 v31, v2
	v_mov_b32_e32 v32, v2
	v_mov_b32_e32 v33, v2
	v_mov_b32_e32 v38, v2
	v_mov_b32_e32 v39, v2
	v_mov_b32_e32 v40, v2
	v_mov_b32_e32 v41, v2
	v_mov_b32_e32 v42, v2
	v_mov_b32_e32 v43, v2
	v_mov_b32_e32 v44, v2
	v_mov_b32_e32 v45, v2
	v_mov_b32_e32 v50, v2
	v_mov_b32_e32 v51, v2
	v_mov_b32_e32 v52, v2
	v_mov_b32_e32 v53, v2
	v_mov_b32_e32 v58, v2
	v_mov_b32_e32 v59, v2
	v_mov_b32_e32 v60, v2
	v_mov_b32_e32 v61, v2
	v_mov_b32_e32 v62, v2
	v_mov_b32_e32 v63, v2
	v_mov_b32_e32 v64, v2
	v_mov_b32_e32 v65, v2
	v_mov_b32_e32 v66, v2
	v_mov_b32_e32 v67, v2
	v_mov_b32_e32 v68, v2
	v_mov_b32_e32 v69, v2
	v_mov_b32_e32 v70, v2
	v_mov_b32_e32 v71, v2
	v_mov_b32_e32 v72, v2
	v_mov_b32_e32 v73, v2
	v_mov_b32_e32 v74, v2
	v_mov_b32_e32 v75, v2
	v_mov_b32_e32 v76, v2
	v_mov_b32_e32 v77, v2
	v_mov_b32_e32 v82, v2
	v_mov_b32_e32 v83, v2
	v_mov_b32_e32 v84, v2
	v_mov_b32_e32 v85, v2
	v_mov_b32_e32 v90, v2
	v_mov_b32_e32 v91, v2
	v_mov_b32_e32 v92, v2
	v_mov_b32_e32 v93, v2
	v_mov_b32_e32 v94, v2
	v_mov_b32_e32 v95, v2
	v_mov_b32_e32 v96, v2
	v_mov_b32_e32 v97, v2
	v_mov_b32_e32 v106, v2
	v_mov_b32_e32 v107, v2
	v_mov_b32_e32 v108, v2
	v_mov_b32_e32 v109, v2
	v_mov_b32_e32 v110, v2
	v_mov_b32_e32 v111, v2
	v_mov_b32_e32 v112, v2
	v_mov_b32_e32 v113, v2
	v_mov_b32_e32 v78, v2
	v_mov_b32_e32 v79, v2
	v_mov_b32_e32 v80, v2
	v_mov_b32_e32 v81, v2
	v_mov_b32_e32 v86, v2
	v_mov_b32_e32 v87, v2
	v_mov_b32_e32 v88, v2
	v_mov_b32_e32 v89, v2
	v_mov_b32_e32 v98, v2
	v_mov_b32_e32 v99, v2
	v_mov_b32_e32 v100, v2
	v_mov_b32_e32 v101, v2
	v_mov_b32_e32 v102, v2
	v_mov_b32_e32 v103, v2
	v_mov_b32_e32 v104, v2
	v_mov_b32_e32 v105, v2
	v_mov_b32_e32 v114, v2
	v_mov_b32_e32 v115, v2
	v_mov_b32_e32 v116, v2
	v_mov_b32_e32 v117, v2
	v_mov_b32_e32 v118, v2
	v_mov_b32_e32 v119, v2
	v_mov_b32_e32 v120, v2
	v_mov_b32_e32 v121, v2
	v_mov_b32_e32 v122, v2
	v_mov_b32_e32 v123, v2
	v_mov_b32_e32 v124, v2
	v_mov_b32_e32 v125, v2
	v_mov_b32_e32 v126, v2
	v_mov_b32_e32 v127, v2
	v_mov_b32_e32 v128, v2
	v_mov_b32_e32 v129, v2
	.p2align	6

; #define PG8_BAR __builtin_amdgcn_s_barrier()
; template <class Epi, class Sched, bool PERM, bool FP8 = false, bool GATHER = false>
; DI void gemm_phase(LAS unsigned char* lds, const unsigned char* wsb, const unsigned lda, const unsigned ldb, const int nt, const Sched& S, const Epi& E) {
;     ...
; #pragma unroll
;         for (int a = 0; a < 2; ++a)
; #pragma unroll
;             for (int b = 0; b < 2; ++b)
; #pragma unroll
;                 for (int m = 0; m < 4; ++m)
; #pragma unroll
;                     for (int n = 0; n < 2; ++n) acc[a][b][m][n] = (f32x4){0.f, 0.f, 0.f, 0.f};
;         cur = nxt; cA = nA; cB = nB; ++ui;
;         if (wr == 1) PG8_BAR;
.LBB0_1341:
	s_and_b64 s[50:51], s[42:43], exec
	v_mov_b32_e32 v66, 0
	s_cselect_b32 s14, s80, s52
	s_add_i32 s83, s52, 0x100
	s_mov_b32 s84, -2
	s_mov_b64 s[50:51], 0
	v_mov_b32_e32 v67, v66
	v_mov_b32_e32 v68, v66
	v_mov_b32_e32 v69, v66
	v_mov_b32_e32 v74, v66
	v_mov_b32_e32 v75, v66
	v_mov_b32_e32 v76, v66
	v_mov_b32_e32 v77, v66
	v_mov_b32_e32 v82, v66
	v_mov_b32_e32 v83, v66
	v_mov_b32_e32 v84, v66
	v_mov_b32_e32 v85, v66
	v_mov_b32_e32 v90, v66
	v_mov_b32_e32 v91, v66
	v_mov_b32_e32 v92, v66
	v_mov_b32_e32 v93, v66
	v_mov_b32_e32 v98, v66
	v_mov_b32_e32 v99, v66
	v_mov_b32_e32 v100, v66
	v_mov_b32_e32 v101, v66
	v_mov_b32_e32 v106, v66
	v_mov_b32_e32 v107, v66
	v_mov_b32_e32 v108, v66
	v_mov_b32_e32 v109, v66
	v_mov_b32_e32 v114, v66
	v_mov_b32_e32 v115, v66
	v_mov_b32_e32 v116, v66
	v_mov_b32_e32 v117, v66
	v_mov_b32_e32 v122, v66
	v_mov_b32_e32 v123, v66
	v_mov_b32_e32 v124, v66
	v_mov_b32_e32 v125, v66
	v_mov_b32_e32 v70, v66
	v_mov_b32_e32 v71, v66
	v_mov_b32_e32 v72, v66
	v_mov_b32_e32 v73, v66
	v_mov_b32_e32 v78, v66
	v_mov_b32_e32 v79, v66
	v_mov_b32_e32 v80, v66
	v_mov_b32_e32 v81, v66
	v_mov_b32_e32 v86, v66
	v_mov_b32_e32 v87, v66
	v_mov_b32_e32 v88, v66
	v_mov_b32_e32 v89, v66
	v_mov_b32_e32 v94, v66
	v_mov_b32_e32 v95, v66
	v_mov_b32_e32 v96, v66
	v_mov_b32_e32 v97, v66
	v_mov_b32_e32 v102, v66
	v_mov_b32_e32 v103, v66
	v_mov_b32_e32 v104, v66
	v_mov_b32_e32 v105, v66
	v_mov_b32_e32 v110, v66
	v_mov_b32_e32 v111, v66
	v_mov_b32_e32 v112, v66
	v_mov_b32_e32 v113, v66
	v_mov_b32_e32 v118, v66
	v_mov_b32_e32 v119, v66
	v_mov_b32_e32 v120, v66
	v_mov_b32_e32 v121, v66
	v_mov_b32_e32 v126, v66
	v_mov_b32_e32 v127, v66
	v_mov_b32_e32 v128, v66
	v_mov_b32_e32 v129, v66
	v_mov_b32_e32 v130, v66
	v_mov_b32_e32 v131, v66
	v_mov_b32_e32 v132, v66
	v_mov_b32_e32 v133, v66
	v_mov_b32_e32 v138, v66
	v_mov_b32_e32 v139, v66
	v_mov_b32_e32 v140, v66
	v_mov_b32_e32 v141, v66
	v_mov_b32_e32 v146, v66
	v_mov_b32_e32 v147, v66
	v_mov_b32_e32 v148, v66
	v_mov_b32_e32 v149, v66
	v_mov_b32_e32 v154, v66
	v_mov_b32_e32 v155, v66
	v_mov_b32_e32 v156, v66
	v_mov_b32_e32 v157, v66
	v_mov_b32_e32 v162, v66
	v_mov_b32_e32 v163, v66
	v_mov_b32_e32 v164, v66
	v_mov_b32_e32 v165, v66
	v_mov_b32_e32 v170, v66
	v_mov_b32_e32 v171, v66
	v_mov_b32_e32 v172, v66
	v_mov_b32_e32 v173, v66
	v_mov_b32_e32 v178, v66
	v_mov_b32_e32 v179, v66
	v_mov_b32_e32 v180, v66
	v_mov_b32_e32 v181, v66
	v_mov_b32_e32 v182, v66
	v_mov_b32_e32 v183, v66
	v_mov_b32_e32 v184, v66
	v_mov_b32_e32 v185, v66
	v_mov_b32_e32 v134, v66
	v_mov_b32_e32 v135, v66
	v_mov_b32_e32 v136, v66
	v_mov_b32_e32 v137, v66
	v_mov_b32_e32 v142, v66
	v_mov_b32_e32 v143, v66
	v_mov_b32_e32 v144, v66
	v_mov_b32_e32 v145, v66
	v_mov_b32_e32 v150, v66
	v_mov_b32_e32 v151, v66
	v_mov_b32_e32 v152, v66
	v_mov_b32_e32 v153, v66
	v_mov_b32_e32 v158, v66
	v_mov_b32_e32 v159, v66
	v_mov_b32_e32 v160, v66
	v_mov_b32_e32 v161, v66
	v_mov_b32_e32 v166, v66
	v_mov_b32_e32 v167, v66
	v_mov_b32_e32 v168, v66
	v_mov_b32_e32 v169, v66
	v_mov_b32_e32 v174, v66
	v_mov_b32_e32 v175, v66
	v_mov_b32_e32 v176, v66
	v_mov_b32_e32 v177, v66
	v_mov_b32_e32 v186, v66
	v_mov_b32_e32 v187, v66
	v_mov_b32_e32 v188, v66
	v_mov_b32_e32 v189, v66
	v_mov_b32_e32 v190, v66
	v_mov_b32_e32 v191, v66
	v_mov_b32_e32 v192, v66
	v_mov_b32_e32 v193, v66
	s_branch .LBB0_1343
	.p2align	6

; #define PG8_BAR __builtin_amdgcn_s_barrier()
; template <class Epi, class Sched, bool PERM, bool FP8 = false, bool GATHER = false>
; DI void gemm_phase(LAS unsigned char* lds, const unsigned char* wsb, const unsigned lda, const unsigned ldb, const int nt, const Sched& S, const Epi& E) {
;     ...
; #pragma unroll
;         for (int a = 0; a < 2; ++a)
; #pragma unroll
;             for (int b = 0; b < 2; ++b)
; #pragma unroll
;                 for (int m = 0; m < 4; ++m)
; #pragma unroll
;                     for (int n = 0; n < 2; ++n) acc[a][b][m][n] = (f32x4){0.f, 0.f, 0.f, 0.f};
;         cur = nxt; cA = nA; cB = nB; ++ui;
;         if (wr == 1) PG8_BAR;
.LBB0_1449:
	s_and_b64 s[24:25], s[20:21], exec
	v_mov_b32_e32 v2, 0
	s_cselect_b32 s69, s61, s68
	s_mov_b32 s70, -2
	s_mov_b32 s71, 0x20080
	v_mov_b32_e32 v3, v2
	v_mov_b32_e32 v4, v2
	v_mov_b32_e32 v5, v2
	v_mov_b32_e32 v6, v2
	v_mov_b32_e32 v7, v2
	v_mov_b32_e32 v8, v2
	v_mov_b32_e32 v9, v2
	v_mov_b32_e32 v14, v2
	v_mov_b32_e32 v15, v2
	v_mov_b32_e32 v16, v2
	v_mov_b32_e32 v17, v2
	v_mov_b32_e32 v22, v2
	v_mov_b32_e32 v23, v2
	v_mov_b32_e32 v24, v2
	v_mov_b32_e32 v25, v2
	v_mov_b32_e32 v30, v2
	v_mov_b32_e32 v31, v2
	v_mov_b32_e32 v32, v2
	v_mov_b32_e32 v33, v2
	v_mov_b32_e32 v38, v2
	v_mov_b32_e32 v39, v2
	v_mov_b32_e32 v40, v2
	v_mov_b32_e32 v41, v2
	v_mov_b32_e32 v46, v2
	v_mov_b32_e32 v47, v2
	v_mov_b32_e32 v48, v2
	v_mov_b32_e32 v49, v2
	v_mov_b32_e32 v54, v2
	v_mov_b32_e32 v55, v2
	v_mov_b32_e32 v56, v2
	v_mov_b32_e32 v57, v2
	v_mov_b32_e32 v10, v2
	v_mov_b32_e32 v11, v2
	v_mov_b32_e32 v12, v2
	v_mov_b32_e32 v13, v2
	v_mov_b32_e32 v18, v2
	v_mov_b32_e32 v19, v2
	v_mov_b32_e32 v20, v2
	v_mov_b32_e32 v21, v2
	v_mov_b32_e32 v26, v2
	v_mov_b32_e32 v27, v2
	v_mov_b32_e32 v28, v2
	v_mov_b32_e32 v29, v2
	v_mov_b32_e32 v34, v2
	v_mov_b32_e32 v35, v2
	v_mov_b32_e32 v36, v2
	v_mov_b32_e32 v37, v2
	v_mov_b32_e32 v42, v2
	v_mov_b32_e32 v43, v2
	v_mov_b32_e32 v44, v2
	v_mov_b32_e32 v45, v2
	v_mov_b32_e32 v50, v2
	v_mov_b32_e32 v51, v2
	v_mov_b32_e32 v52, v2
	v_mov_b32_e32 v53, v2
	v_mov_b32_e32 v58, v2
	v_mov_b32_e32 v59, v2
	v_mov_b32_e32 v60, v2
	v_mov_b32_e32 v61, v2
	v_mov_b32_e32 v62, v2
	v_mov_b32_e32 v63, v2
	v_mov_b32_e32 v64, v2
	v_mov_b32_e32 v65, v2
	v_mov_b32_e32 v66, v2
	v_mov_b32_e32 v67, v2
	v_mov_b32_e32 v68, v2
	v_mov_b32_e32 v69, v2
	v_mov_b32_e32 v70, v2
	v_mov_b32_e32 v71, v2
	v_mov_b32_e32 v72, v2
	v_mov_b32_e32 v73, v2
	v_mov_b32_e32 v78, v2
	v_mov_b32_e32 v79, v2
	v_mov_b32_e32 v80, v2
	v_mov_b32_e32 v81, v2
	v_mov_b32_e32 v86, v2
	v_mov_b32_e32 v87, v2
	v_mov_b32_e32 v88, v2
	v_mov_b32_e32 v89, v2
	v_mov_b32_e32 v98, v2
	v_mov_b32_e32 v99, v2
	v_mov_b32_e32 v100, v2
	v_mov_b32_e32 v101, v2
	v_mov_b32_e32 v102, v2
	v_mov_b32_e32 v103, v2
	v_mov_b32_e32 v104, v2
	v_mov_b32_e32 v105, v2
	v_mov_b32_e32 v106, v2
	v_mov_b32_e32 v107, v2
	v_mov_b32_e32 v108, v2
	v_mov_b32_e32 v109, v2
	v_mov_b32_e32 v110, v2
	v_mov_b32_e32 v111, v2
	v_mov_b32_e32 v112, v2
	v_mov_b32_e32 v113, v2
	v_mov_b32_e32 v74, v2
	v_mov_b32_e32 v75, v2
	v_mov_b32_e32 v76, v2
	v_mov_b32_e32 v77, v2
	v_mov_b32_e32 v82, v2
	v_mov_b32_e32 v83, v2
	v_mov_b32_e32 v84, v2
	v_mov_b32_e32 v85, v2
	v_mov_b32_e32 v90, v2
	v_mov_b32_e32 v91, v2
	v_mov_b32_e32 v92, v2
	v_mov_b32_e32 v93, v2
	v_mov_b32_e32 v94, v2
	v_mov_b32_e32 v95, v2
	v_mov_b32_e32 v96, v2
	v_mov_b32_e32 v97, v2
	v_mov_b32_e32 v114, v2
	v_mov_b32_e32 v115, v2
	v_mov_b32_e32 v116, v2
	v_mov_b32_e32 v117, v2
	v_mov_b32_e32 v118, v2
	v_mov_b32_e32 v119, v2
	v_mov_b32_e32 v120, v2
	v_mov_b32_e32 v121, v2
	v_mov_b32_e32 v122, v2
	v_mov_b32_e32 v123, v2
	v_mov_b32_e32 v124, v2
	v_mov_b32_e32 v125, v2
	v_mov_b32_e32 v126, v2
	v_mov_b32_e32 v127, v2
	v_mov_b32_e32 v128, v2
	v_mov_b32_e32 v129, v2
	.p2align	6

; #define PG8_BAR __builtin_amdgcn_s_barrier()
; template <class Epi, class Sched, bool PERM, bool FP8 = false, bool GATHER = false>
; DI void gemm_phase(LAS unsigned char* lds, const unsigned char* wsb, const unsigned lda, const unsigned ldb, const int nt, const Sched& S, const Epi& E) {
;     ...
; #pragma unroll
;         for (int a = 0; a < 2; ++a)
; #pragma unroll
;             for (int b = 0; b < 2; ++b)
; #pragma unroll
;                 for (int m = 0; m < 4; ++m)
; #pragma unroll
;                     for (int n = 0; n < 2; ++n) acc[a][b][m][n] = (f32x4){0.f, 0.f, 0.f, 0.f};
;         cur = nxt; cA = nA; cB = nB; ++ui;
;         if (wr == 1) PG8_BAR;
.LBB0_1625:
	v_mov_b32_e32 v2, 0
	s_add_i32 s6, s9, 0x100
	s_add_i32 s7, s8, 0x20080
	s_mov_b32 s8, -2
	v_mov_b32_e32 v3, v2
	v_mov_b32_e32 v4, v2
	v_mov_b32_e32 v5, v2
	v_mov_b32_e32 v6, v2
	v_mov_b32_e32 v7, v2
	v_mov_b32_e32 v8, v2
	v_mov_b32_e32 v9, v2
	v_mov_b32_e32 v18, v2
	v_mov_b32_e32 v19, v2
	v_mov_b32_e32 v20, v2
	v_mov_b32_e32 v21, v2
	v_mov_b32_e32 v22, v2
	v_mov_b32_e32 v23, v2
	v_mov_b32_e32 v24, v2
	v_mov_b32_e32 v25, v2
	v_mov_b32_e32 v34, v2
	v_mov_b32_e32 v35, v2
	v_mov_b32_e32 v36, v2
	v_mov_b32_e32 v37, v2
	v_mov_b32_e32 v38, v2
	v_mov_b32_e32 v39, v2
	v_mov_b32_e32 v40, v2
	v_mov_b32_e32 v41, v2
	v_mov_b32_e32 v50, v2
	v_mov_b32_e32 v51, v2
	v_mov_b32_e32 v52, v2
	v_mov_b32_e32 v53, v2
	v_mov_b32_e32 v54, v2
	v_mov_b32_e32 v55, v2
	v_mov_b32_e32 v56, v2
	v_mov_b32_e32 v57, v2
	v_mov_b32_e32 v10, v2
	v_mov_b32_e32 v11, v2
	v_mov_b32_e32 v12, v2
	v_mov_b32_e32 v13, v2
	v_mov_b32_e32 v14, v2
	v_mov_b32_e32 v15, v2
	v_mov_b32_e32 v16, v2
	v_mov_b32_e32 v17, v2
	v_mov_b32_e32 v26, v2
	v_mov_b32_e32 v27, v2
	v_mov_b32_e32 v28, v2
	v_mov_b32_e32 v29, v2
	v_mov_b32_e32 v30, v2
	v_mov_b32_e32 v31, v2
	v_mov_b32_e32 v32, v2
	v_mov_b32_e32 v33, v2
	v_mov_b32_e32 v42, v2
	v_mov_b32_e32 v43, v2
	v_mov_b32_e32 v44, v2
	v_mov_b32_e32 v45, v2
	v_mov_b32_e32 v46, v2
	v_mov_b32_e32 v47, v2
	v_mov_b32_e32 v48, v2
	v_mov_b32_e32 v49, v2
	v_mov_b32_e32 v58, v2
	v_mov_b32_e32 v59, v2
	v_mov_b32_e32 v60, v2
	v_mov_b32_e32 v61, v2
	v_mov_b32_e32 v62, v2
	v_mov_b32_e32 v63, v2
	v_mov_b32_e32 v64, v2
	v_mov_b32_e32 v65, v2
	v_mov_b32_e32 v66, v2
	v_mov_b32_e32 v67, v2
	v_mov_b32_e32 v68, v2
	v_mov_b32_e32 v69, v2
	v_mov_b32_e32 v70, v2
	v_mov_b32_e32 v71, v2
	v_mov_b32_e32 v72, v2
	v_mov_b32_e32 v73, v2
	v_mov_b32_e32 v82, v2
	v_mov_b32_e32 v83, v2
	v_mov_b32_e32 v84, v2
	v_mov_b32_e32 v85, v2
	v_mov_b32_e32 v86, v2
	v_mov_b32_e32 v87, v2
	v_mov_b32_e32 v88, v2
	v_mov_b32_e32 v89, v2
	v_mov_b32_e32 v98, v2
	v_mov_b32_e32 v99, v2
	v_mov_b32_e32 v100, v2
	v_mov_b32_e32 v101, v2
	v_mov_b32_e32 v102, v2
	v_mov_b32_e32 v103, v2
	v_mov_b32_e32 v104, v2
	v_mov_b32_e32 v105, v2
	v_mov_b32_e32 v114, v2
	v_mov_b32_e32 v115, v2
	v_mov_b32_e32 v116, v2
	v_mov_b32_e32 v117, v2
	v_mov_b32_e32 v118, v2
	v_mov_b32_e32 v119, v2
	v_mov_b32_e32 v120, v2
	v_mov_b32_e32 v121, v2
	v_mov_b32_e32 v74, v2
	v_mov_b32_e32 v75, v2
	v_mov_b32_e32 v76, v2
	v_mov_b32_e32 v77, v2
	v_mov_b32_e32 v78, v2
	v_mov_b32_e32 v79, v2
	v_mov_b32_e32 v80, v2
	v_mov_b32_e32 v81, v2
	v_mov_b32_e32 v90, v2
	v_mov_b32_e32 v91, v2
	v_mov_b32_e32 v92, v2
	v_mov_b32_e32 v93, v2
	v_mov_b32_e32 v94, v2
	v_mov_b32_e32 v95, v2
	v_mov_b32_e32 v96, v2
	v_mov_b32_e32 v97, v2
	v_mov_b32_e32 v106, v2
	v_mov_b32_e32 v107, v2
	v_mov_b32_e32 v108, v2
	v_mov_b32_e32 v109, v2
	v_mov_b32_e32 v110, v2
	v_mov_b32_e32 v111, v2
	v_mov_b32_e32 v112, v2
	v_mov_b32_e32 v113, v2
	v_mov_b32_e32 v122, v2
	v_mov_b32_e32 v123, v2
	v_mov_b32_e32 v124, v2
	v_mov_b32_e32 v125, v2
	v_mov_b32_e32 v126, v2
	v_mov_b32_e32 v127, v2
	v_mov_b32_e32 v128, v2
	v_mov_b32_e32 v129, v2
	.p2align	6

; #define PG8_BAR __builtin_amdgcn_s_barrier()
; template <class Epi, class Sched, bool PERM, bool FP8 = false, bool GATHER = false>
; DI void gemm_phase(LAS unsigned char* lds, const unsigned char* wsb, const unsigned lda, const unsigned ldb, const int nt, const Sched& S, const Epi& E) {
;     ...
; #pragma unroll
;         for (int a = 0; a < 2; ++a)
; #pragma unroll
;             for (int b = 0; b < 2; ++b)
; #pragma unroll
;                 for (int m = 0; m < 4; ++m)
; #pragma unroll
;                     for (int n = 0; n < 2; ++n) acc[a][b][m][n] = (f32x4){0.f, 0.f, 0.f, 0.f};
;         cur = nxt; cA = nA; cB = nB; ++ui;
;         if (wr == 1) PG8_BAR;
.LBB0_1801:
	v_mov_b32_e32 v2, 0
	s_addk_i32 s8, 0x100
	s_add_i32 s20, s22, 0x20080
	s_mov_b32 s21, -2
	v_mov_b32_e32 v3, v2
	v_mov_b32_e32 v4, v2
	v_mov_b32_e32 v5, v2
	v_mov_b32_e32 v6, v2
	v_mov_b32_e32 v7, v2
	v_mov_b32_e32 v8, v2
	v_mov_b32_e32 v9, v2
	v_mov_b32_e32 v14, v2
	v_mov_b32_e32 v15, v2
	v_mov_b32_e32 v16, v2
	v_mov_b32_e32 v17, v2
	v_mov_b32_e32 v22, v2
	v_mov_b32_e32 v23, v2
	v_mov_b32_e32 v24, v2
	v_mov_b32_e32 v25, v2
	v_mov_b32_e32 v30, v2
	v_mov_b32_e32 v31, v2
	v_mov_b32_e32 v32, v2
	v_mov_b32_e32 v33, v2
	v_mov_b32_e32 v38, v2
	v_mov_b32_e32 v39, v2
	v_mov_b32_e32 v40, v2
	v_mov_b32_e32 v41, v2
	v_mov_b32_e32 v46, v2
	v_mov_b32_e32 v47, v2
	v_mov_b32_e32 v48, v2
	v_mov_b32_e32 v49, v2
	v_mov_b32_e32 v54, v2
	v_mov_b32_e32 v55, v2
	v_mov_b32_e32 v56, v2
	v_mov_b32_e32 v57, v2
	v_mov_b32_e32 v10, v2
	v_mov_b32_e32 v11, v2
	v_mov_b32_e32 v12, v2
	v_mov_b32_e32 v13, v2
	v_mov_b32_e32 v18, v2
	v_mov_b32_e32 v19, v2
	v_mov_b32_e32 v20, v2
	v_mov_b32_e32 v21, v2
	v_mov_b32_e32 v26, v2
	v_mov_b32_e32 v27, v2
	v_mov_b32_e32 v28, v2
	v_mov_b32_e32 v29, v2
	v_mov_b32_e32 v34, v2
	v_mov_b32_e32 v35, v2
	v_mov_b32_e32 v36, v2
	v_mov_b32_e32 v37, v2
	v_mov_b32_e32 v42, v2
	v_mov_b32_e32 v43, v2
	v_mov_b32_e32 v44, v2
	v_mov_b32_e32 v45, v2
	v_mov_b32_e32 v50, v2
	v_mov_b32_e32 v51, v2
	v_mov_b32_e32 v52, v2
	v_mov_b32_e32 v53, v2
	v_mov_b32_e32 v58, v2
	v_mov_b32_e32 v59, v2
	v_mov_b32_e32 v60, v2
	v_mov_b32_e32 v61, v2
	v_mov_b32_e32 v62, v2
	v_mov_b32_e32 v63, v2
	v_mov_b32_e32 v64, v2
	v_mov_b32_e32 v65, v2
	v_mov_b32_e32 v66, v2
	v_mov_b32_e32 v67, v2
	v_mov_b32_e32 v68, v2
	v_mov_b32_e32 v69, v2
	v_mov_b32_e32 v70, v2
	v_mov_b32_e32 v71, v2
	v_mov_b32_e32 v72, v2
	v_mov_b32_e32 v73, v2
	v_mov_b32_e32 v78, v2
	v_mov_b32_e32 v79, v2
	v_mov_b32_e32 v80, v2
	v_mov_b32_e32 v81, v2
	v_mov_b32_e32 v86, v2
	v_mov_b32_e32 v87, v2
	v_mov_b32_e32 v88, v2
	v_mov_b32_e32 v89, v2
	v_mov_b32_e32 v94, v2
	v_mov_b32_e32 v95, v2
	v_mov_b32_e32 v96, v2
	v_mov_b32_e32 v97, v2
	v_mov_b32_e32 v102, v2
	v_mov_b32_e32 v103, v2
	v_mov_b32_e32 v104, v2
	v_mov_b32_e32 v105, v2
	v_mov_b32_e32 v110, v2
	v_mov_b32_e32 v111, v2
	v_mov_b32_e32 v112, v2
	v_mov_b32_e32 v113, v2
	v_mov_b32_e32 v118, v2
	v_mov_b32_e32 v119, v2
	v_mov_b32_e32 v120, v2
	v_mov_b32_e32 v121, v2
	v_mov_b32_e32 v74, v2
	v_mov_b32_e32 v75, v2
	v_mov_b32_e32 v76, v2
	v_mov_b32_e32 v77, v2
	v_mov_b32_e32 v82, v2
	v_mov_b32_e32 v83, v2
	v_mov_b32_e32 v84, v2
	v_mov_b32_e32 v85, v2
	v_mov_b32_e32 v90, v2
	v_mov_b32_e32 v91, v2
	v_mov_b32_e32 v92, v2
	v_mov_b32_e32 v93, v2
	v_mov_b32_e32 v98, v2
	v_mov_b32_e32 v99, v2
	v_mov_b32_e32 v100, v2
	v_mov_b32_e32 v101, v2
	v_mov_b32_e32 v106, v2
	v_mov_b32_e32 v107, v2
	v_mov_b32_e32 v108, v2
	v_mov_b32_e32 v109, v2
	v_mov_b32_e32 v114, v2
	v_mov_b32_e32 v115, v2
	v_mov_b32_e32 v116, v2
	v_mov_b32_e32 v117, v2
	v_mov_b32_e32 v122, v2
	v_mov_b32_e32 v123, v2
	v_mov_b32_e32 v124, v2
	v_mov_b32_e32 v125, v2
	v_mov_b32_e32 v126, v2
	v_mov_b32_e32 v127, v2
	v_mov_b32_e32 v128, v2
	v_mov_b32_e32 v129, v2
	.p2align	6

; DI void attn_unit_d8(unsigned char* lds, const AttnArgs& a) {
;     ...
;     f32x16 o0[2], o1[2];
; #pragma unroll
;     for (int d = 0; d < 2; ++d) { o0[d] = (f32x16){}; o1[d] = (f32x16){}; }
;     f32x4 l0 = {0.f, 0.f, 0.f, 0.f}, l1 = {0.f, 0.f, 0.f, 0.f};
;     constexpr int D8_SLOT = 2 * 64 * A8_PITCH;
;     u32x2 kreg0, vreg0, kreg1, vreg1;
;     auto gload = [&](int t, u32x2& kreg, u32x2& vreg) __attribute__((always_inline)) {
;         const unsigned char* kp = (t < 64) ? a.klat8 + (size_t)(t * 64 + lrow) * 256 : a.kctx8 + (size_t)((t - 64) * 64 + lrow) * 256;
;         kreg = *(const u32x2*)(kp + 8 * lch);
;         vreg = *(const u32x2*)(vsrc + (size_t)t * 64);
;     };
;     auto lstore = [&](int slot, const u32x2& kreg, const u32x2& vreg) __attribute__((always_inline)) { unsigned char* b = lds + slot * D8_SLOT;
;         *(u32x2*)(b + ldst) = kreg; *(unsigned*)(b + ldv) = vreg.x; *(unsigned*)(b + ldv + 32) = vreg.y; };
;     auto rd32 = [&](const unsigned char* p) __attribute__((always_inline)) -> v8i { const u32x4 lo = *(const u32x4*)p, hi = *(const u32x4*)(p + 16);
;         return (v8i){(int)lo.x, (int)lo.y, (int)lo.z, (int)lo.w, (int)hi.x, (int)hi.y, (int)hi.z, (int)hi.w}; };
;     auto expsum = [&](f32x16& sc, f32x4& l) __attribute__((always_inline)) {
; #pragma unroll
;         for (int i = 0; i < 16; ++i) sc[i] = __builtin_amdgcn_exp2f(sc[i]);
; #pragma unroll
;         for (int i = 0; i < 4; ++i) l += (f32x4){sc[4 * i], sc[4 * i + 1], sc[4 * i + 2], sc[4 * i + 3]};
;     };
;     auto pack8 = [&](const f32x16& s0, const f32x16& s1) __attribute__((always_inline)) -> v8i { v8i p;
; #pragma unroll
;         for (int g = 0; g < 4; ++g) { p[g] = (int)pk4_fp8_div16(s0[4 * g], s0[4 * g + 1], s0[4 * g + 2], s0[4 * g + 3]); p[4 + g] = (int)pk4_fp8_div16(s1[4 * g], s1[4 * g + 1], s1[4 * g + 2], s1[4 * g + 3]); }
;         return p; };
;     auto pack4 = [&](const f32x16& sc, v8i& p, const int o) __attribute__((always_inline)) {
; #pragma unroll
;         for (int g = 0; g < 4; ++g) p[o + g] = (int)pk4_fp8_div16(sc[4 * g], sc[4 * g + 1], sc[4 * g + 2], sc[4 * g + 3]); };
;     auto qk = [&](const unsigned char* Kb, int hh, f32x16& sa, f32x16& sb) __attribute__((always_inline)) { const v8i kf = rd32(Kb + koff + hh * 32 * A8_PITCH);
;         sa = mfma8(kf, qfa, (f32x16){}); sb = mfma8(kf, qfb, (f32x16){}); };
.LBB0_1887:
	s_and_b32 s61, s46, 1
	s_lshl_b32 s61, s61, 3
	s_sub_i32 s61, 0, s61
	s_ashr_i32 s21, s20, 31
	s_lshl_b64 s[20:21], s[20:21], 8
	s_add_u32 s8, s24, s20
	s_addc_u32 s20, s25, s21
	s_add_u32 s8, s8, s47
	s_addc_u32 s21, s20, 0
	s_add_u32 s20, s8, 0x800000
	v_mov_b32_e32 v2, 0
	s_addc_u32 s21, s21, 0
	s_mov_b32 s23, 0
	s_mov_b32 s22, -2
	v_mov_b32_e32 v138, 0
	v_mov_b32_e32 v139, 0
	v_mov_b32_e32 v140, 0
	v_mov_b32_e32 v141, 0
	v_mov_b32_e32 v142, 0
	v_mov_b32_e32 v143, 0
	v_mov_b32_e32 v144, 0
	v_mov_b32_e32 v145, 0
	v_mov_b32_e32 v130, 0
	v_mov_b32_e32 v131, 0
	v_mov_b32_e32 v132, 0
	v_mov_b32_e32 v133, 0
	v_mov_b32_e32 v134, 0
	v_mov_b32_e32 v135, 0
	v_mov_b32_e32 v136, 0
	v_mov_b32_e32 v137, 0
	v_mov_b32_e32 v154, 0
	v_mov_b32_e32 v155, 0
	v_mov_b32_e32 v156, 0
	v_mov_b32_e32 v157, 0
	v_mov_b32_e32 v158, 0
	v_mov_b32_e32 v159, 0
	v_mov_b32_e32 v160, 0
	v_mov_b32_e32 v161, 0
	v_mov_b32_e32 v146, 0
	v_mov_b32_e32 v147, 0
	v_mov_b32_e32 v148, 0
	v_mov_b32_e32 v149, 0
	v_mov_b32_e32 v150, 0
	v_mov_b32_e32 v151, 0
	v_mov_b32_e32 v152, 0
	v_mov_b32_e32 v153, 0
	v_mov_b32_e32 v3, v2
	v_mov_b32_e32 v4, v2
	v_mov_b32_e32 v5, v2
	v_mov_b32_e32 v6, v2
	v_mov_b32_e32 v7, v2
	v_mov_b32_e32 v8, v2
	v_mov_b32_e32 v9, v2
	v_mov_b32_e32 v10, v2
	v_mov_b32_e32 v11, v2
	v_mov_b32_e32 v12, v2
	v_mov_b32_e32 v13, v2
	v_mov_b32_e32 v14, v2
	v_mov_b32_e32 v15, v2
	v_mov_b32_e32 v16, v2
	v_mov_b32_e32 v17, v2
	v_mov_b32_e32 v18, v2
	v_mov_b32_e32 v19, v2
	v_mov_b32_e32 v20, v2
	v_mov_b32_e32 v21, v2
	v_mov_b32_e32 v22, v2
	v_mov_b32_e32 v23, v2
	v_mov_b32_e32 v24, v2
	v_mov_b32_e32 v25, v2
	v_mov_b32_e32 v26, v2
	v_mov_b32_e32 v27, v2
	v_mov_b32_e32 v28, v2
	v_mov_b32_e32 v29, v2
	v_mov_b32_e32 v30, v2
	v_mov_b32_e32 v31, v2
	v_mov_b32_e32 v32, v2
	v_mov_b32_e32 v33, v2
	v_mov_b32_e32 v50, v2
	v_mov_b32_e32 v51, v2
	v_mov_b32_e32 v52, v2
	v_mov_b32_e32 v53, v2
	v_mov_b32_e32 v54, v2
	v_mov_b32_e32 v55, v2
	v_mov_b32_e32 v56, v2
	v_mov_b32_e32 v57, v2
	v_mov_b32_e32 v58, v2
	v_mov_b32_e32 v59, v2
	v_mov_b32_e32 v60, v2
	v_mov_b32_e32 v61, v2
	v_mov_b32_e32 v62, v2
	v_mov_b32_e32 v63, v2
	v_mov_b32_e32 v64, v2
	v_mov_b32_e32 v65, v2
	v_mov_b32_e32 v34, v2
	v_mov_b32_e32 v35, v2
	v_mov_b32_e32 v36, v2
	v_mov_b32_e32 v37, v2
	v_mov_b32_e32 v38, v2
	v_mov_b32_e32 v39, v2
	v_mov_b32_e32 v40, v2
	v_mov_b32_e32 v41, v2
	v_mov_b32_e32 v42, v2
	v_mov_b32_e32 v43, v2
	v_mov_b32_e32 v44, v2
	v_mov_b32_e32 v45, v2
	v_mov_b32_e32 v46, v2
	v_mov_b32_e32 v47, v2
	v_mov_b32_e32 v48, v2
	v_mov_b32_e32 v49, v2
	v_mov_b32_e32 v188, v2
	v_mov_b32_e32 v189, v2
	v_mov_b32_e32 v186, v2
	v_mov_b32_e32 v187, v2
	v_mov_b32_e32 v192, v2
	v_mov_b32_e32 v193, v2
	v_mov_b32_e32 v190, v2
	v_mov_b32_e32 v191, v2
	.p2align	6

; DI void attn_unit_a8(unsigned char* lds, const AttnArgs& a) {
;     ...
;     {
;         int t = a.t0;
;         if (wrider)
;             for (int j = 0; j < AT_NWT; ++j, t += 2) { step(t, kregB, vregB, kregA, vregA, sx0, sx1, sy0, sy1, 1, j); step(t + 1, kregA, vregA, kregB, vregB, sy0, sy1, sx0, sx1, 2, j); }
;         for (; t < a.t1; t += 2) {
;             step(t, kregB, vregB, kregA, vregA, sx0, sx1, sy0, sy1, 0, 0);
;             if (t + 1 < a.t1) step(t + 1, kregA, vregA, kregB, vregB, sy0, sy1, sx0, sx1, 0, 0);
;             else { sx0 = sy0; sx1 = sy1; }
;         }
.LBB0_1933:
	s_lshl_b32 s10, s75, 8
	s_ashr_i32 s11, s10, 31
	s_lshl_b64 s[10:11], s[10:11], 7
	s_add_u32 s8, s54, s10
	s_addc_u32 s10, s55, s11
	s_add_u32 s8, s8, s77
	s_addc_u32 s10, s10, 0
	s_add_u32 s12, s8, 0x400000
	s_addc_u32 s13, s10, 0
	s_mov_b32 s14, 0
	v_mov_b64_e32 v[80:81], v[64:65]
	v_mov_b64_e32 v[78:79], v[62:63]
	v_mov_b64_e32 v[76:77], v[60:61]
	v_mov_b64_e32 v[74:75], v[58:59]
	v_mov_b64_e32 v[72:73], v[56:57]
	v_mov_b64_e32 v[70:71], v[54:55]
	v_mov_b64_e32 v[68:69], v[52:53]
	v_mov_b64_e32 v[66:67], v[50:51]
	v_mov_b64_e32 v[96:97], v[48:49]
	v_mov_b64_e32 v[94:95], v[46:47]
	v_mov_b64_e32 v[92:93], v[44:45]
	v_mov_b64_e32 v[90:91], v[42:43]
	v_mov_b64_e32 v[88:89], v[40:41]
	v_mov_b64_e32 v[86:87], v[38:39]
	v_mov_b64_e32 v[84:85], v[36:37]
	v_mov_b64_e32 v[82:83], v[34:35]
	v_mov_b32_e32 v236, v130
	v_ashrrev_i32_e32 v237, 31, v130
	v_lshlrev_b64 v[236:237], 7, v[236:237]
	v_lshl_add_u64 v[236:237], v[236:237], 0, v[132:133]
	.p2align	6

; #define PG8_BAR __builtin_amdgcn_s_barrier()
; template <class Epi, class Sched, bool PERM, bool FP8 = false, bool GATHER = false>
; DI void gemm_phase(LAS unsigned char* lds, const unsigned char* wsb, const unsigned lda, const unsigned ldb, const int nt, const Sched& S, const Epi& E) {
;     ...
; #pragma unroll
;         for (int a = 0; a < 2; ++a)
; #pragma unroll
;             for (int b = 0; b < 2; ++b)
; #pragma unroll
;                 for (int m = 0; m < 4; ++m)
; #pragma unroll
;                     for (int n = 0; n < 2; ++n) acc[a][b][m][n] = (f32x4){0.f, 0.f, 0.f, 0.f};
;         cur = nxt; cA = nA; cB = nB; ++ui;
;         if (wr == 1) PG8_BAR;
.LBB0_2115:
	v_mov_b32_e32 v2, 0
	s_add_i32 s71, s71, 0x20080
	s_addk_i32 s72, 0x100
	s_mov_b32 s73, -2
	v_mov_b32_e32 v3, v2
	v_mov_b32_e32 v4, v2
	v_mov_b32_e32 v5, v2
	v_mov_b32_e32 v6, v2
	v_mov_b32_e32 v7, v2
	v_mov_b32_e32 v8, v2
	v_mov_b32_e32 v9, v2
	v_mov_b32_e32 v14, v2
	v_mov_b32_e32 v15, v2
	v_mov_b32_e32 v16, v2
	v_mov_b32_e32 v17, v2
	v_mov_b32_e32 v22, v2
	v_mov_b32_e32 v23, v2
	v_mov_b32_e32 v24, v2
	v_mov_b32_e32 v25, v2
	v_mov_b32_e32 v30, v2
	v_mov_b32_e32 v31, v2
	v_mov_b32_e32 v32, v2
	v_mov_b32_e32 v33, v2
	v_mov_b32_e32 v38, v2
	v_mov_b32_e32 v39, v2
	v_mov_b32_e32 v40, v2
	v_mov_b32_e32 v41, v2
	v_mov_b32_e32 v46, v2
	v_mov_b32_e32 v47, v2
	v_mov_b32_e32 v48, v2
	v_mov_b32_e32 v49, v2
	v_mov_b32_e32 v54, v2
	v_mov_b32_e32 v55, v2
	v_mov_b32_e32 v56, v2
	v_mov_b32_e32 v57, v2
	v_mov_b32_e32 v10, v2
	v_mov_b32_e32 v11, v2
	v_mov_b32_e32 v12, v2
	v_mov_b32_e32 v13, v2
	v_mov_b32_e32 v18, v2
	v_mov_b32_e32 v19, v2
	v_mov_b32_e32 v20, v2
	v_mov_b32_e32 v21, v2
	v_mov_b32_e32 v26, v2
	v_mov_b32_e32 v27, v2
	v_mov_b32_e32 v28, v2
	v_mov_b32_e32 v29, v2
	v_mov_b32_e32 v34, v2
	v_mov_b32_e32 v35, v2
	v_mov_b32_e32 v36, v2
	v_mov_b32_e32 v37, v2
	v_mov_b32_e32 v42, v2
	v_mov_b32_e32 v43, v2
	v_mov_b32_e32 v44, v2
	v_mov_b32_e32 v45, v2
	v_mov_b32_e32 v50, v2
	v_mov_b32_e32 v51, v2
	v_mov_b32_e32 v52, v2
	v_mov_b32_e32 v53, v2
	v_mov_b32_e32 v58, v2
	v_mov_b32_e32 v59, v2
	v_mov_b32_e32 v60, v2
	v_mov_b32_e32 v61, v2
	v_mov_b32_e32 v62, v2
	v_mov_b32_e32 v63, v2
	v_mov_b32_e32 v64, v2
	v_mov_b32_e32 v65, v2
	v_mov_b32_e32 v66, v2
	v_mov_b32_e32 v67, v2
	v_mov_b32_e32 v68, v2
	v_mov_b32_e32 v69, v2
	v_mov_b32_e32 v70, v2
	v_mov_b32_e32 v71, v2
	v_mov_b32_e32 v72, v2
	v_mov_b32_e32 v73, v2
	v_mov_b32_e32 v78, v2
	v_mov_b32_e32 v79, v2
	v_mov_b32_e32 v80, v2
	v_mov_b32_e32 v81, v2
	v_mov_b32_e32 v86, v2
	v_mov_b32_e32 v87, v2
	v_mov_b32_e32 v88, v2
	v_mov_b32_e32 v89, v2
	v_mov_b32_e32 v94, v2
	v_mov_b32_e32 v95, v2
	v_mov_b32_e32 v96, v2
	v_mov_b32_e32 v97, v2
	v_mov_b32_e32 v102, v2
	v_mov_b32_e32 v103, v2
	v_mov_b32_e32 v104, v2
	v_mov_b32_e32 v105, v2
	v_mov_b32_e32 v110, v2
	v_mov_b32_e32 v111, v2
	v_mov_b32_e32 v112, v2
	v_mov_b32_e32 v113, v2
	v_mov_b32_e32 v118, v2
	v_mov_b32_e32 v119, v2
	v_mov_b32_e32 v120, v2
	v_mov_b32_e32 v121, v2
	v_mov_b32_e32 v74, v2
	v_mov_b32_e32 v75, v2
	v_mov_b32_e32 v76, v2
	v_mov_b32_e32 v77, v2
	v_mov_b32_e32 v82, v2
	v_mov_b32_e32 v83, v2
	v_mov_b32_e32 v84, v2
	v_mov_b32_e32 v85, v2
	v_mov_b32_e32 v90, v2
	v_mov_b32_e32 v91, v2
	v_mov_b32_e32 v92, v2
	v_mov_b32_e32 v93, v2
	v_mov_b32_e32 v98, v2
	v_mov_b32_e32 v99, v2
	v_mov_b32_e32 v100, v2
	v_mov_b32_e32 v101, v2
	v_mov_b32_e32 v106, v2
	v_mov_b32_e32 v107, v2
	v_mov_b32_e32 v108, v2
	v_mov_b32_e32 v109, v2
	v_mov_b32_e32 v114, v2
	v_mov_b32_e32 v115, v2
	v_mov_b32_e32 v116, v2
	v_mov_b32_e32 v117, v2
	v_mov_b32_e32 v122, v2
	v_mov_b32_e32 v123, v2
	v_mov_b32_e32 v124, v2
	v_mov_b32_e32 v125, v2
	v_mov_b32_e32 v126, v2
	v_mov_b32_e32 v127, v2
	v_mov_b32_e32 v128, v2
	v_mov_b32_e32 v129, v2
	.p2align	6

; #define PG8_BAR __builtin_amdgcn_s_barrier()
; template <class Epi, class Sched, bool PERM, bool FP8 = false, bool GATHER = false>
; DI void gemm_phase(LAS unsigned char* lds, const unsigned char* wsb, const unsigned lda, const unsigned ldb, const int nt, const Sched& S, const Epi& E) {
;     ...
; #pragma unroll
;         for (int a = 0; a < 2; ++a)
; #pragma unroll
;             for (int b = 0; b < 2; ++b)
; #pragma unroll
;                 for (int m = 0; m < 4; ++m)
; #pragma unroll
;                     for (int n = 0; n < 2; ++n) acc[a][b][m][n] = (f32x4){0.f, 0.f, 0.f, 0.f};
;         cur = nxt; cA = nA; cB = nB; ++ui;
;         if (wr == 1) PG8_BAR;
.LBB0_2543:
	s_and_b64 s[44:45], s[40:41], exec
	v_mov_b32_e32 v66, 0
	s_cselect_b32 s12, s78, s46
	s_add_i32 s80, s46, 0x100
	s_mov_b32 s81, -2
	s_mov_b64 s[44:45], 0
	v_mov_b32_e32 v67, v66
	v_mov_b32_e32 v68, v66
	v_mov_b32_e32 v69, v66
	v_mov_b32_e32 v74, v66
	v_mov_b32_e32 v75, v66
	v_mov_b32_e32 v76, v66
	v_mov_b32_e32 v77, v66
	v_mov_b32_e32 v82, v66
	v_mov_b32_e32 v83, v66
	v_mov_b32_e32 v84, v66
	v_mov_b32_e32 v85, v66
	v_mov_b32_e32 v90, v66
	v_mov_b32_e32 v91, v66
	v_mov_b32_e32 v92, v66
	v_mov_b32_e32 v93, v66
	v_mov_b32_e32 v98, v66
	v_mov_b32_e32 v99, v66
	v_mov_b32_e32 v100, v66
	v_mov_b32_e32 v101, v66
	v_mov_b32_e32 v106, v66
	v_mov_b32_e32 v107, v66
	v_mov_b32_e32 v108, v66
	v_mov_b32_e32 v109, v66
	v_mov_b32_e32 v114, v66
	v_mov_b32_e32 v115, v66
	v_mov_b32_e32 v116, v66
	v_mov_b32_e32 v117, v66
	v_mov_b32_e32 v122, v66
	v_mov_b32_e32 v123, v66
	v_mov_b32_e32 v124, v66
	v_mov_b32_e32 v125, v66
	v_mov_b32_e32 v70, v66
	v_mov_b32_e32 v71, v66
	v_mov_b32_e32 v72, v66
	v_mov_b32_e32 v73, v66
	v_mov_b32_e32 v78, v66
	v_mov_b32_e32 v79, v66
	v_mov_b32_e32 v80, v66
	v_mov_b32_e32 v81, v66
	v_mov_b32_e32 v86, v66
	v_mov_b32_e32 v87, v66
	v_mov_b32_e32 v88, v66
	v_mov_b32_e32 v89, v66
	v_mov_b32_e32 v94, v66
	v_mov_b32_e32 v95, v66
	v_mov_b32_e32 v96, v66
	v_mov_b32_e32 v97, v66
	v_mov_b32_e32 v102, v66
	v_mov_b32_e32 v103, v66
	v_mov_b32_e32 v104, v66
	v_mov_b32_e32 v105, v66
	v_mov_b32_e32 v110, v66
	v_mov_b32_e32 v111, v66
	v_mov_b32_e32 v112, v66
	v_mov_b32_e32 v113, v66
	v_mov_b32_e32 v118, v66
	v_mov_b32_e32 v119, v66
	v_mov_b32_e32 v120, v66
	v_mov_b32_e32 v121, v66
	v_mov_b32_e32 v126, v66
	v_mov_b32_e32 v127, v66
	v_mov_b32_e32 v128, v66
	v_mov_b32_e32 v129, v66
	v_mov_b32_e32 v130, v66
	v_mov_b32_e32 v131, v66
	v_mov_b32_e32 v132, v66
	v_mov_b32_e32 v133, v66
	v_mov_b32_e32 v138, v66
	v_mov_b32_e32 v139, v66
	v_mov_b32_e32 v140, v66
	v_mov_b32_e32 v141, v66
	v_mov_b32_e32 v146, v66
	v_mov_b32_e32 v147, v66
	v_mov_b32_e32 v148, v66
	v_mov_b32_e32 v149, v66
	v_mov_b32_e32 v154, v66
	v_mov_b32_e32 v155, v66
	v_mov_b32_e32 v156, v66
	v_mov_b32_e32 v157, v66
	v_mov_b32_e32 v162, v66
	v_mov_b32_e32 v163, v66
	v_mov_b32_e32 v164, v66
	v_mov_b32_e32 v165, v66
	v_mov_b32_e32 v170, v66
	v_mov_b32_e32 v171, v66
	v_mov_b32_e32 v172, v66
	v_mov_b32_e32 v173, v66
	v_mov_b32_e32 v178, v66
	v_mov_b32_e32 v179, v66
	v_mov_b32_e32 v180, v66
	v_mov_b32_e32 v181, v66
	v_mov_b32_e32 v182, v66
	v_mov_b32_e32 v183, v66
	v_mov_b32_e32 v184, v66
	v_mov_b32_e32 v185, v66
	v_mov_b32_e32 v134, v66
	v_mov_b32_e32 v135, v66
	v_mov_b32_e32 v136, v66
	v_mov_b32_e32 v137, v66
	v_mov_b32_e32 v142, v66
	v_mov_b32_e32 v143, v66
	v_mov_b32_e32 v144, v66
	v_mov_b32_e32 v145, v66
	v_mov_b32_e32 v150, v66
	v_mov_b32_e32 v151, v66
	v_mov_b32_e32 v152, v66
	v_mov_b32_e32 v153, v66
	v_mov_b32_e32 v158, v66
	v_mov_b32_e32 v159, v66
	v_mov_b32_e32 v160, v66
	v_mov_b32_e32 v161, v66
	v_mov_b32_e32 v166, v66
	v_mov_b32_e32 v167, v66
	v_mov_b32_e32 v168, v66
	v_mov_b32_e32 v169, v66
	v_mov_b32_e32 v174, v66
	v_mov_b32_e32 v175, v66
	v_mov_b32_e32 v176, v66
	v_mov_b32_e32 v177, v66
	v_mov_b32_e32 v186, v66
	v_mov_b32_e32 v187, v66
	v_mov_b32_e32 v188, v66
	v_mov_b32_e32 v189, v66
	v_mov_b32_e32 v190, v66
	v_mov_b32_e32 v191, v66
	v_mov_b32_e32 v192, v66
	v_mov_b32_e32 v193, v66
	s_branch .LBB0_2545
	.p2align	6

; #define PG8_BAR __builtin_amdgcn_s_barrier()
; template <class Epi, class Sched, bool PERM, bool FP8 = false, bool GATHER = false>
; DI void gemm_phase(LAS unsigned char* lds, const unsigned char* wsb, const unsigned lda, const unsigned ldb, const int nt, const Sched& S, const Epi& E) {
;     ...
; #pragma unroll
;         for (int a = 0; a < 2; ++a)
; #pragma unroll
;             for (int b = 0; b < 2; ++b)
; #pragma unroll
;                 for (int m = 0; m < 4; ++m)
; #pragma unroll
;                     for (int n = 0; n < 2; ++n) acc[a][b][m][n] = (f32x4){0.f, 0.f, 0.f, 0.f};
;         cur = nxt; cA = nA; cB = nB; ++ui;
;         if (wr == 1) PG8_BAR;
.LBB0_2651:
	s_and_b64 s[24:25], s[20:21], exec
	v_mov_b32_e32 v2, 0
	s_cselect_b32 s65, s59, s64
	s_mov_b32 s66, -2
	s_mov_b32 s67, 0x20080
	v_mov_b32_e32 v3, v2
	v_mov_b32_e32 v4, v2
	v_mov_b32_e32 v5, v2
	v_mov_b32_e32 v6, v2
	v_mov_b32_e32 v7, v2
	v_mov_b32_e32 v8, v2
	v_mov_b32_e32 v9, v2
	v_mov_b32_e32 v14, v2
	v_mov_b32_e32 v15, v2
	v_mov_b32_e32 v16, v2
	v_mov_b32_e32 v17, v2
	v_mov_b32_e32 v22, v2
	v_mov_b32_e32 v23, v2
	v_mov_b32_e32 v24, v2
	v_mov_b32_e32 v25, v2
	v_mov_b32_e32 v30, v2
	v_mov_b32_e32 v31, v2
	v_mov_b32_e32 v32, v2
	v_mov_b32_e32 v33, v2
	v_mov_b32_e32 v38, v2
	v_mov_b32_e32 v39, v2
	v_mov_b32_e32 v40, v2
	v_mov_b32_e32 v41, v2
	v_mov_b32_e32 v46, v2
	v_mov_b32_e32 v47, v2
	v_mov_b32_e32 v48, v2
	v_mov_b32_e32 v49, v2
	v_mov_b32_e32 v54, v2
	v_mov_b32_e32 v55, v2
	v_mov_b32_e32 v56, v2
	v_mov_b32_e32 v57, v2
	v_mov_b32_e32 v10, v2
	v_mov_b32_e32 v11, v2
	v_mov_b32_e32 v12, v2
	v_mov_b32_e32 v13, v2
	v_mov_b32_e32 v18, v2
	v_mov_b32_e32 v19, v2
	v_mov_b32_e32 v20, v2
	v_mov_b32_e32 v21, v2
	v_mov_b32_e32 v26, v2
	v_mov_b32_e32 v27, v2
	v_mov_b32_e32 v28, v2
	v_mov_b32_e32 v29, v2
	v_mov_b32_e32 v34, v2
	v_mov_b32_e32 v35, v2
	v_mov_b32_e32 v36, v2
	v_mov_b32_e32 v37, v2
	v_mov_b32_e32 v42, v2
	v_mov_b32_e32 v43, v2
	v_mov_b32_e32 v44, v2
	v_mov_b32_e32 v45, v2
	v_mov_b32_e32 v50, v2
	v_mov_b32_e32 v51, v2
	v_mov_b32_e32 v52, v2
	v_mov_b32_e32 v53, v2
	v_mov_b32_e32 v58, v2
	v_mov_b32_e32 v59, v2
	v_mov_b32_e32 v60, v2
	v_mov_b32_e32 v61, v2
	v_mov_b32_e32 v62, v2
	v_mov_b32_e32 v63, v2
	v_mov_b32_e32 v64, v2
	v_mov_b32_e32 v65, v2
	v_mov_b32_e32 v66, v2
	v_mov_b32_e32 v67, v2
	v_mov_b32_e32 v68, v2
	v_mov_b32_e32 v69, v2
	v_mov_b32_e32 v70, v2
	v_mov_b32_e32 v71, v2
	v_mov_b32_e32 v72, v2
	v_mov_b32_e32 v73, v2
	v_mov_b32_e32 v78, v2
	v_mov_b32_e32 v79, v2
	v_mov_b32_e32 v80, v2
	v_mov_b32_e32 v81, v2
	v_mov_b32_e32 v86, v2
	v_mov_b32_e32 v87, v2
	v_mov_b32_e32 v88, v2
	v_mov_b32_e32 v89, v2
	v_mov_b32_e32 v98, v2
	v_mov_b32_e32 v99, v2
	v_mov_b32_e32 v100, v2
	v_mov_b32_e32 v101, v2
	v_mov_b32_e32 v102, v2
	v_mov_b32_e32 v103, v2
	v_mov_b32_e32 v104, v2
	v_mov_b32_e32 v105, v2
	v_mov_b32_e32 v106, v2
	v_mov_b32_e32 v107, v2
	v_mov_b32_e32 v108, v2
	v_mov_b32_e32 v109, v2
	v_mov_b32_e32 v110, v2
	v_mov_b32_e32 v111, v2
	v_mov_b32_e32 v112, v2
	v_mov_b32_e32 v113, v2
	v_mov_b32_e32 v74, v2
	v_mov_b32_e32 v75, v2
	v_mov_b32_e32 v76, v2
	v_mov_b32_e32 v77, v2
	v_mov_b32_e32 v82, v2
	v_mov_b32_e32 v83, v2
	v_mov_b32_e32 v84, v2
	v_mov_b32_e32 v85, v2
	v_mov_b32_e32 v90, v2
	v_mov_b32_e32 v91, v2
	v_mov_b32_e32 v92, v2
	v_mov_b32_e32 v93, v2
	v_mov_b32_e32 v94, v2
	v_mov_b32_e32 v95, v2
	v_mov_b32_e32 v96, v2
	v_mov_b32_e32 v97, v2
	v_mov_b32_e32 v114, v2
	v_mov_b32_e32 v115, v2
	v_mov_b32_e32 v116, v2
	v_mov_b32_e32 v117, v2
	v_mov_b32_e32 v118, v2
	v_mov_b32_e32 v119, v2
	v_mov_b32_e32 v120, v2
	v_mov_b32_e32 v121, v2
	v_mov_b32_e32 v122, v2
	v_mov_b32_e32 v123, v2
	v_mov_b32_e32 v124, v2
	v_mov_b32_e32 v125, v2
	v_mov_b32_e32 v126, v2
	v_mov_b32_e32 v127, v2
	v_mov_b32_e32 v128, v2
	v_mov_b32_e32 v129, v2
	.p2align	6
